# pipelined weight-conversion loads carry the nt (streaming) hint: the f32 weights are read once and no longer displace the attention operands in L2
# speedup vs baseline: 1.0252x; 1.0117x over previous
; #define LAS __attribute__((address_space(3)))
; __device__ __forceinline__ void tr_tile8(const float* __restrict__ src, int N, const float* __restrict__ ksc, float wscale, unsigned char* __restrict__ dst, int ldd, int k0, int n0, int drow0, LAS unsigned* tl, int tid) {
;     const int c4 = (tid & 15) * 4, kq = tid >> 4;
;     const float* s0 = src + (size_t)(k0 + 4 * kq) * N + n0 + c4;
;     f32x4 a = *(const f32x4*)s0, b = *(const f32x4*)(s0 + N), c = *(const f32x4*)(s0 + 2 * (size_t)N), d = *(const f32x4*)(s0 + 3 * (size_t)N);
.Lcv1_proc:
	s_mov_b32 s101, 0
	s_cmp_lt_i32 s100, 0
	s_cbranch_scc1 .Lcv1_nx
	s_cmp_lt_i32 s23, 30
	s_cbranch_scc0 .Lcv1_nx
	s_cmp_eq_u32 s50, 0x100
	s_cbranch_scc0 .Lcv1_nx
	s_mov_b64 vcc, 0x800000
	v_lshl_add_u64 v[64:65], v[64:65], 0, vcc
	s_lshl_b64 s[48:49], s[36:37], 2
	v_lshl_add_u64 v[72:73], v[64:65], 0, s[48:49]
	global_load_dwordx4 v[80:83], v[64:65], off nt
	global_load_dwordx4 v[84:87], v[72:73], off nt
	v_lshl_add_u64 v[72:73], v[72:73], 0, s[48:49]
	v_lshl_add_u64 v[74:75], v[72:73], 0, s[48:49]
	global_load_dwordx4 v[88:91], v[72:73], off nt
	global_load_dwordx4 v[92:95], v[74:75], off nt
	s_mov_b32 s101, 1
